# speedup vs baseline: 1.0250x; 1.0015x over previous
.LBB0_4:
	s_or_b64 exec, exec, s[6:7]
	s_ashr_i32 s3, s2, 31
	s_lshl_b64 s[6:7], s[2:3], 16
	v_and_b32_e32 v1, 63, v0
	s_waitcnt lgkmcnt(0)
	s_add_u32 s4, s4, s6
	v_lshrrev_b32_e32 v66, 6, v0
	s_addc_u32 s5, s5, s7
	v_lshlrev_b32_e32 v2, 4, v1
	v_mov_b32_e32 v3, 0
	v_lshl_add_u64 v[4:5], s[4:5], 0, v[2:3]
	v_lshlrev_b32_e32 v2, 14, v66
	v_lshl_add_u64 v[2:3], v[4:5], 0, v[2:3]
	s_movk_i32 s3, 0x1000
	v_add_co_u32_e32 v68, vcc, s3, v2
	s_movk_i32 s3, 0x2000
	s_nop 0
	v_addc_co_u32_e32 v69, vcc, 0, v3, vcc
	v_add_co_u32_e32 v70, vcc, s3, v2
	global_load_dwordx4 v[62:65], v[2:3], off nt
	global_load_dwordx4 v[58:61], v[2:3], off offset:1024 nt
	global_load_dwordx4 v[50:53], v[2:3], off offset:2048 nt
	global_load_dwordx4 v[46:49], v[2:3], off offset:3072 nt
	v_addc_co_u32_e32 v71, vcc, 0, v3, vcc
	v_add_co_u32_e32 v72, vcc, 0x3000, v2
	global_load_dwordx4 v[42:45], v[68:69], off offset:1024 nt
	global_load_dwordx4 v[34:37], v[68:69], off offset:2048 nt
	global_load_dwordx4 v[30:33], v[70:71], off nt
	global_load_dwordx4 v[26:29], v[70:71], off offset:1024 nt
	global_load_dwordx4 v[22:25], v[70:71], off offset:2048 nt
	global_load_dwordx4 v[18:21], v[70:71], off offset:3072 nt
	v_addc_co_u32_e32 v73, vcc, 0, v3, vcc
	global_load_dwordx4 v[38:41], v[68:69], off offset:3072 nt
	global_load_dwordx4 v[14:17], v[72:73], off nt
	global_load_dwordx4 v[10:13], v[72:73], off offset:1024 nt
	global_load_dwordx4 v[6:9], v[72:73], off offset:2048 nt
	global_load_dwordx4 v[54:57], v[70:71], off offset:-4096 nt
	global_load_dwordx4 v[2:5], v[72:73], off offset:3072 nt
	s_cmp_lt_u32 s2, 8
	v_cmp_eq_u32_e32 vcc, 0, v0
	s_cselect_b64 s[4:5], -1, 0
	s_and_b64 s[6:7], s[4:5], vcc
	s_and_saveexec_b64 s[4:5], s[6:7]
	s_cbranch_execz .LBB0_6
.LBB0_6:
	s_or_b64 exec, exec, s[4:5]
	s_waitcnt vmcnt(15)
	v_add_f32_e32 v68, v62, v63
	v_add_f32_e32 v69, v64, v65
	v_add_f32_e32 v68, v68, v69
	s_waitcnt vmcnt(14)
	v_add_f32_e32 v69, v58, v59
	v_add_f32_e32 v70, v60, v61
	v_add_f32_e32 v69, v69, v70
	s_waitcnt vmcnt(13)
	v_add_f32_e32 v70, v50, v51
	v_add_f32_e32 v71, v52, v53
	v_add_f32_e32 v70, v70, v71
	s_waitcnt vmcnt(12)
	v_add_f32_e32 v71, v46, v47
	v_add_f32_e32 v72, v48, v49
	v_add_f32_e32 v71, v71, v72
	s_waitcnt vmcnt(1)
	v_add_f32_e32 v72, v54, v55
	v_add_f32_e32 v73, v56, v57
	v_add_f32_e32 v72, v72, v73
	v_add_f32_e32 v73, v42, v43
	v_add_f32_e32 v74, v44, v45
	v_add_f32_e32 v73, v73, v74
	v_add_f32_e32 v74, v34, v35
	v_add_f32_e32 v75, v36, v37
	v_add_f32_e32 v74, v74, v75
	v_add_f32_e32 v75, v38, v39
	v_add_f32_e32 v76, v40, v41
	v_add_f32_e32 v75, v75, v76
	v_add_f32_e32 v76, v30, v31
	v_add_f32_e32 v77, v32, v33
	v_add_f32_e32 v76, v76, v77
	v_add_f32_e32 v77, v26, v27
	v_add_f32_e32 v78, v28, v29
	v_add_f32_e32 v77, v77, v78
	v_mul_f32_e32 v67, v63, v63
	v_add_f32_e32 v68, v68, v69
	v_mul_f32_e32 v69, v51, v51
	v_add_f32_e32 v74, v74, v75
	v_mul_f32_e32 v75, v31, v31
	v_add_f32_e32 v76, v76, v77
	v_mul_f32_e32 v77, v23, v23
	v_fmac_f32_e32 v67, v62, v62
	v_fmac_f32_e32 v69, v50, v50
	v_fmac_f32_e32 v75, v30, v30
	v_fmac_f32_e32 v77, v22, v22
	v_fmac_f32_e32 v67, v64, v64
	v_fmac_f32_e32 v69, v52, v52
	v_fmac_f32_e32 v75, v32, v32
	v_fmac_f32_e32 v77, v24, v24
	v_add_f32_e32 v78, v22, v23
	v_add_f32_e32 v79, v24, v25
	v_mbcnt_lo_u32_b32 v86, -1, 0
	v_fmac_f32_e32 v67, v65, v65
	v_fmac_f32_e32 v69, v53, v53
	v_fmac_f32_e32 v75, v33, v33
	v_fmac_f32_e32 v77, v25, v25
	v_add_f32_e32 v78, v78, v79
	v_add_f32_e32 v79, v18, v19
	v_add_f32_e32 v80, v20, v21
	v_mbcnt_hi_u32_b32 v86, -1, v86
	v_fmac_f32_e32 v67, v58, v58
	v_fmac_f32_e32 v69, v46, v46
	v_fmac_f32_e32 v75, v26, v26
	v_fmac_f32_e32 v77, v18, v18
	v_add_f32_e32 v79, v79, v80
	v_add_f32_e32 v80, v14, v15
	v_add_f32_e32 v81, v16, v17
	v_and_b32_e32 v88, 64, v86
	v_fmac_f32_e32 v67, v59, v59
	v_fmac_f32_e32 v69, v47, v47
	v_fmac_f32_e32 v75, v27, v27
	v_fmac_f32_e32 v77, v19, v19
	v_add_f32_e32 v80, v80, v81
	v_add_f32_e32 v81, v10, v11
	v_add_f32_e32 v82, v12, v13
	v_xor_b32_e32 v87, 32, v86
	v_add_u32_e32 v88, 64, v88
	v_fmac_f32_e32 v67, v60, v60
	v_fmac_f32_e32 v69, v48, v48
	v_add_f32_e32 v70, v70, v71
	v_mul_f32_e32 v71, v55, v55
	v_fmac_f32_e32 v75, v28, v28
	v_fmac_f32_e32 v77, v20, v20
	v_add_f32_e32 v78, v78, v79
	v_mul_f32_e32 v79, v15, v15
	v_add_f32_e32 v81, v81, v82
	v_add_f32_e32 v82, v6, v7
	v_add_f32_e32 v83, v8, v9
	v_and_b32_e32 v85, 32, v0
	v_cmp_lt_i32_e32 vcc, v87, v88
	v_fmac_f32_e32 v67, v61, v61
	v_fmac_f32_e32 v69, v49, v49
	v_fmac_f32_e32 v71, v54, v54
	v_fmac_f32_e32 v75, v29, v29
	v_fmac_f32_e32 v77, v21, v21
	v_fmac_f32_e32 v79, v14, v14
	v_add_f32_e32 v82, v82, v83
	s_waitcnt vmcnt(0)
	v_add_f32_e32 v83, v2, v3
	v_add_f32_e32 v84, v4, v5
	v_cndmask_b32_e32 v87, v86, v87, vcc
	v_cmp_eq_u32_e32 vcc, 0, v85
	v_fmac_f32_e32 v71, v56, v56
	v_add_f32_e32 v72, v72, v73
	v_mul_f32_e32 v73, v35, v35
	v_fmac_f32_e32 v79, v16, v16
	v_add_f32_e32 v80, v80, v81
	v_mul_f32_e32 v81, v7, v7
	v_lshlrev_b32_e32 v87, 2, v87
	v_cndmask_b32_e32 v85, v75, v67, vcc
	v_cndmask_b32_e32 v67, v67, v75, vcc
	v_add_f32_e32 v75, v83, v84
	v_cndmask_b32_e32 v84, v76, v68, vcc
	v_cndmask_b32_e32 v68, v68, v76, vcc
	v_cndmask_b32_e32 v76, v69, v77, vcc
	v_fmac_f32_e32 v71, v57, v57
	v_fmac_f32_e32 v73, v34, v34
	v_fmac_f32_e32 v79, v17, v17
	v_fmac_f32_e32 v81, v6, v6
	ds_bpermute_b32 v76, v87, v76
	v_fmac_f32_e32 v71, v42, v42
	v_fmac_f32_e32 v73, v36, v36
	v_fmac_f32_e32 v79, v10, v10
	v_fmac_f32_e32 v81, v8, v8
	v_fmac_f32_e32 v71, v43, v43
	v_fmac_f32_e32 v73, v37, v37
	v_fmac_f32_e32 v79, v11, v11
	v_fmac_f32_e32 v81, v9, v9
	ds_bpermute_b32 v67, v87, v67
	v_fmac_f32_e32 v71, v44, v44
	v_fmac_f32_e32 v73, v38, v38
	v_fmac_f32_e32 v79, v12, v12
	v_fmac_f32_e32 v81, v2, v2
	v_fmac_f32_e32 v71, v45, v45
	v_fmac_f32_e32 v73, v39, v39
	v_fmac_f32_e32 v79, v13, v13
	v_fmac_f32_e32 v81, v3, v3
	v_cndmask_b32_e32 v69, v77, v69, vcc
	v_fmac_f32_e32 v73, v40, v40
	v_fmac_f32_e32 v81, v4, v4
	s_waitcnt lgkmcnt(1)
	v_add_f32_e32 v69, v69, v76
	v_cndmask_b32_e32 v76, v79, v71, vcc
	v_cndmask_b32_e32 v71, v71, v79, vcc
	v_fmac_f32_e32 v73, v41, v41
	v_fmac_f32_e32 v81, v5, v5
	ds_bpermute_b32 v71, v87, v71
	s_waitcnt lgkmcnt(1)
	v_add_f32_e32 v67, v85, v67
	v_cndmask_b32_e32 v85, v70, v78, vcc
	v_cndmask_b32_e32 v70, v78, v70, vcc
	v_cndmask_b32_e32 v78, v73, v81, vcc
	v_cndmask_b32_e32 v77, v72, v80, vcc
	ds_bpermute_b32 v78, v87, v78
	ds_bpermute_b32 v77, v87, v77
	s_waitcnt lgkmcnt(2)
	v_add_f32_e32 v71, v76, v71
	v_xor_b32_e32 v76, 16, v86
	v_add_f32_e32 v75, v82, v75
	v_and_b32_e32 v82, 16, v0
	v_cndmask_b32_e32 v73, v81, v73, vcc
	v_cmp_lt_i32_e64 s[4:5], v76, v88
	v_cndmask_b32_e32 v72, v80, v72, vcc
	s_waitcnt lgkmcnt(1)
	v_add_f32_e32 v73, v73, v78
	v_cndmask_b32_e64 v76, v86, v76, s[4:5]
	v_cmp_eq_u32_e64 s[4:5], 0, v82
	s_waitcnt lgkmcnt(0)
	v_add_f32_e32 v72, v72, v77
	v_lshlrev_b32_e32 v76, 2, v76
	v_cndmask_b32_e64 v77, v71, v67, s[4:5]
	v_cndmask_b32_e64 v67, v67, v71, s[4:5]
	v_cndmask_b32_e64 v71, v69, v73, s[4:5]
	ds_bpermute_b32 v67, v76, v67
	ds_bpermute_b32 v71, v76, v71
	v_and_b32_e32 v83, 8, v0
	v_cndmask_b32_e64 v69, v73, v69, s[4:5]
	v_cmp_eq_u32_e64 s[6:7], 0, v83
	s_waitcnt lgkmcnt(1)
	v_add_f32_e32 v67, v77, v67
	s_waitcnt lgkmcnt(0)
	v_add_f32_e32 v69, v69, v71
	v_cndmask_b32_e64 v71, v69, v67, s[6:7]
	v_cndmask_b32_e64 v67, v67, v69, s[6:7]
	v_xor_b32_e32 v69, 8, v86
	v_cmp_lt_i32_e64 s[8:9], v69, v88
	ds_bpermute_b32 v68, v87, v68
	v_cndmask_b32_e32 v78, v74, v75, vcc
	v_cndmask_b32_e64 v69, v86, v69, s[8:9]
	v_lshlrev_b32_e32 v69, 2, v69
	ds_bpermute_b32 v67, v69, v67
	ds_bpermute_b32 v85, v87, v85
	ds_bpermute_b32 v78, v87, v78
	s_waitcnt lgkmcnt(3)
	v_add_f32_e32 v68, v84, v68
	v_cndmask_b32_e32 v73, v75, v74, vcc
	v_cndmask_b32_e64 v74, v68, v72, s[4:5]
	s_waitcnt lgkmcnt(2)
	v_add_f32_e32 v67, v71, v67
	v_xor_b32_e32 v71, 4, v86
	ds_bpermute_b32 v74, v76, v74
	v_cmp_lt_i32_e32 vcc, v71, v88
	s_waitcnt lgkmcnt(2)
	v_add_f32_e32 v70, v70, v85
	s_waitcnt lgkmcnt(1)
	v_add_f32_e32 v73, v73, v78
	v_cndmask_b32_e32 v71, v86, v71, vcc
	v_lshlrev_b32_e32 v71, 2, v71
	ds_bpermute_b32 v75, v71, v67
	v_cndmask_b32_e64 v68, v72, v68, s[4:5]
	v_cndmask_b32_e64 v72, v70, v73, s[4:5]
	ds_bpermute_b32 v72, v76, v72
	s_waitcnt lgkmcnt(2)
	v_add_f32_e32 v68, v68, v74
	v_xor_b32_e32 v74, 2, v86
	v_cmp_lt_i32_e32 vcc, v74, v88
	s_waitcnt lgkmcnt(1)
	v_add_f32_e32 v67, v67, v75
	v_cndmask_b32_e64 v70, v73, v70, s[4:5]
	v_cndmask_b32_e32 v74, v86, v74, vcc
	v_lshlrev_b32_e32 v74, 2, v74
	ds_bpermute_b32 v75, v74, v67
	s_waitcnt lgkmcnt(1)
	v_add_f32_e32 v70, v70, v72
	v_cndmask_b32_e64 v72, v68, v70, s[6:7]
	ds_bpermute_b32 v69, v69, v72
	v_xor_b32_e32 v72, 1, v86
	v_cmp_lt_i32_e32 vcc, v72, v88
	s_waitcnt lgkmcnt(1)
	v_add_f32_e32 v67, v67, v75
	v_cndmask_b32_e64 v68, v70, v68, s[6:7]
	v_cndmask_b32_e32 v72, v86, v72, vcc
	v_lshlrev_b32_e32 v72, 2, v72
	ds_bpermute_b32 v73, v72, v67
	s_mov_b32 s3, 0xf800000
	s_waitcnt lgkmcnt(1)
	v_add_f32_e32 v68, v68, v69
	ds_bpermute_b32 v69, v71, v68
	s_waitcnt lgkmcnt(1)
	v_add_f32_e32 v67, v67, v73
	v_mul_f32_e32 v70, 0x4f800000, v67
	v_cmp_gt_f32_e32 vcc, s3, v67
	s_waitcnt lgkmcnt(0)
	v_add_f32_e32 v69, v68, v69
	ds_bpermute_b32 v71, v74, v69
	v_cndmask_b32_e32 v67, v67, v70, vcc
	v_sqrt_f32_e32 v70, v67
	s_waitcnt lgkmcnt(0)
	v_add_f32_e32 v69, v69, v71
	v_add_u32_e32 v68, -1, v70
	v_fma_f32 v73, -v68, v70, v67
	v_cmp_ge_f32_e64 s[4:5], 0, v73
	v_add_u32_e32 v73, 1, v70
	s_nop 0
	v_cndmask_b32_e64 v68, v70, v68, s[4:5]
	v_fma_f32 v70, -v73, v70, v67
	v_cmp_lt_f32_e64 s[4:5], 0, v70
	s_nop 1
	v_cndmask_b32_e64 v68, v68, v73, s[4:5]
	v_mul_f32_e32 v70, 0x37800000, v68
	v_cndmask_b32_e32 v68, v68, v70, vcc
	v_mov_b32_e32 v70, 0x260
	v_cmp_class_f32_e32 vcc, v67, v70
	ds_bpermute_b32 v70, v72, v69
	s_nop 0
	v_cndmask_b32_e32 v67, v68, v67, vcc
	v_max_f32_e32 v68, 0x322bcc77, v67
	v_div_scale_f32 v67, s[4:5], v68, v68, 1.0
	v_rcp_f32_e32 v73, v67
	s_load_dwordx2 s[4:5], s[0:1], 0x8
	v_fma_f32 v71, -v67, v73, 1.0
	v_fmac_f32_e32 v73, v71, v73
	v_div_scale_f32 v71, vcc, 1.0, v68, 1.0
	v_mul_f32_e32 v72, v71, v73
	v_fma_f32 v74, -v67, v72, v71
	v_fmac_f32_e32 v72, v74, v73
	v_fma_f32 v67, -v67, v72, v71
	v_div_fmas_f32 v71, v67, v73, v72
	v_and_b32_e32 v67, 7, v0
	v_cmp_ne_u32_e32 vcc, 0, v67
	v_lshlrev_b32_e32 v67, 3, v66
	s_and_saveexec_b64 s[6:7], vcc
	s_xor_b64 s[6:7], exec, s[6:7]
	v_lshlrev_b32_e32 v67, 3, v66
	s_or_saveexec_b64 s[6:7], s[6:7]
	v_div_fixup_f32 v66, v71, v68, 1.0
	s_xor_b64 exec, exec, s[6:7]
	s_cbranch_execz .LBB0_10
	s_load_dwordx2 s[0:1], s[0:1], 0x10
	s_waitcnt lgkmcnt(0)
	v_add_f32_e32 v68, v69, v70
	v_mul_f32_e32 v70, v68, v66
	s_lshl_b32 s3, s2, 5
	v_lshrrev_b32_e32 v68, 3, v1
	v_or3_b32 v68, v67, s3, v68
	v_ashrrev_i32_e32 v69, 31, v68
	v_lshl_add_u64 v[68:69], v[68:69], 2, s[0:1]
	global_store_dword v[68:69], v70, off
